# GDN section c rewritten by hand: all 25 LDS fragment/decay reads issued up front, 4 MFMA accumulate chains, branch-free masking; same arithmetic
# speedup vs baseline: 1.0378x; 1.0040x over previous
.Lgpf_done_next:
	v_and_b32_e32 v0, 15, v215
	v_lshrrev_b32_e32 v1, 4, v215
	v_readlane_b32 s0, v253, 51
	v_readlane_b32 s1, v253, 52
	v_add_u32_e32 v2, s9, v0
	v_mul_u32_u24_e32 v3, 0x110, v2
	v_lshl_add_u32 v3, v1, 4, v3
	v_mul_u32_u24_e32 v4, 0x110, v0
	v_lshl_add_u32 v4, v1, 4, v4
	v_add_u32_e32 v3, s0, v3
	v_add_u32_e32 v4, s1, v4
	s_lshl_b32 s20, s9, 2
	s_add_i32 s20, s20, 0x1c400
	v_lshl_add_u32 v5, v1, 4, s20
	v_lshlrev_b32_e32 v6, 2, v0
	v_add_u32_e32 v6, 0x1c400, v6
	ds_read_b128 v[40:43], v3
	ds_read_b128 v[44:47], v3 offset:64
	ds_read_b128 v[48:51], v3 offset:128
	ds_read_b128 v[52:55], v3 offset:192
	ds_read_b128 v[56:59], v4
	ds_read_b128 v[60:63], v4 offset:64
	ds_read_b128 v[64:67], v4 offset:128
	ds_read_b128 v[68:71], v4 offset:192
	ds_read_b128 v[144:147], v5
	ds_read_b32 v136, v6
	ds_read_b32 v137, v6 offset:64
	ds_read_b32 v138, v6 offset:128
	ds_read_b32 v139, v6 offset:192
	ds_read_b128 v[72:75], v4 offset:4352
	ds_read_b128 v[76:79], v4 offset:4416
	ds_read_b128 v[80:83], v4 offset:4480
	ds_read_b128 v[84:87], v4 offset:4544
	ds_read_b128 v[88:91], v4 offset:8704
	ds_read_b128 v[92:95], v4 offset:8768
	ds_read_b128 v[96:99], v4 offset:8832
	ds_read_b128 v[100:103], v4 offset:8896
	ds_read_b128 v[104:107], v4 offset:13056
	ds_read_b128 v[108:111], v4 offset:13120
	ds_read_b128 v[112:115], v4 offset:13184
	ds_read_b128 v[116:119], v4 offset:13248
	v_add_u32_e32 v9, 16, v0
	v_add_u32_e32 v10, 32, v0
	v_add_u32_e32 v11, 48, v0
	v_lshl_add_u32 v12, v1, 2, s9
	v_add_u32_e32 v13, 1, v12
	v_add_u32_e32 v14, 2, v12
	v_add_u32_e32 v15, 3, v12
	s_and_b32 s34, s56, 0x80000000
	s_xor_b32 s34, s34, 0x3fb8aa3b
	s_waitcnt lgkmcnt(15)
	v_mfma_f32_16x16x32_bf16 v[120:123], v[40:43], v[56:59], 0
	v_mfma_f32_16x16x32_bf16 v[120:123], v[44:47], v[60:63], v[120:123]
	v_mfma_f32_16x16x32_bf16 v[120:123], v[48:51], v[64:67], v[120:123]
	v_mfma_f32_16x16x32_bf16 v[120:123], v[52:55], v[68:71], v[120:123]
	v_sub_f32_e32 v148, v144, v136
	v_sub_f32_e32 v149, v145, v136
	v_sub_f32_e32 v150, v146, v136
	v_sub_f32_e32 v151, v147, v136
	v_mul_f32_e32 v148, s34, v148
	v_mul_f32_e32 v149, s34, v149
	v_mul_f32_e32 v150, s34, v150
	v_mul_f32_e32 v151, s34, v151
	v_exp_f32_e32 v148, v148
	v_exp_f32_e32 v149, v149
	v_exp_f32_e32 v150, v150
	v_exp_f32_e32 v151, v151
	s_waitcnt lgkmcnt(8)
	v_mfma_f32_16x16x32_bf16 v[124:127], v[40:43], v[72:75], 0
	v_mfma_f32_16x16x32_bf16 v[124:127], v[44:47], v[76:79], v[124:127]
	v_mfma_f32_16x16x32_bf16 v[124:127], v[48:51], v[80:83], v[124:127]
	v_mfma_f32_16x16x32_bf16 v[124:127], v[52:55], v[84:87], v[124:127]
	v_mul_f32_e32 v148, v120, v148
	v_mul_f32_e32 v149, v121, v149
	v_mul_f32_e32 v150, v122, v150
	v_mul_f32_e32 v151, v123, v151
	v_sub_f32_e32 v152, v144, v137
	v_sub_f32_e32 v153, v145, v137
	v_sub_f32_e32 v154, v146, v137
	v_sub_f32_e32 v155, v147, v137
	v_mul_f32_e32 v152, s34, v152
	v_mul_f32_e32 v153, s34, v153
	v_mul_f32_e32 v154, s34, v154
	v_mul_f32_e32 v155, s34, v155
	v_exp_f32_e32 v152, v152
	v_exp_f32_e32 v153, v153
	v_exp_f32_e32 v154, v154
	v_exp_f32_e32 v155, v155
	s_waitcnt lgkmcnt(4)
	v_mfma_f32_16x16x32_bf16 v[128:131], v[40:43], v[88:91], 0
	v_mfma_f32_16x16x32_bf16 v[128:131], v[44:47], v[92:95], v[128:131]
	v_mfma_f32_16x16x32_bf16 v[128:131], v[48:51], v[96:99], v[128:131]
	v_mfma_f32_16x16x32_bf16 v[128:131], v[52:55], v[100:103], v[128:131]
	v_mul_f32_e32 v152, v124, v152
	v_mul_f32_e32 v153, v125, v153
	v_mul_f32_e32 v154, v126, v154
	v_mul_f32_e32 v155, v127, v155
	v_sub_f32_e32 v156, v144, v138
	v_sub_f32_e32 v157, v145, v138
	v_sub_f32_e32 v158, v146, v138
	v_sub_f32_e32 v159, v147, v138
	v_mul_f32_e32 v156, s34, v156
	v_mul_f32_e32 v157, s34, v157
	v_mul_f32_e32 v158, s34, v158
	v_mul_f32_e32 v159, s34, v159
	v_exp_f32_e32 v156, v156
	v_exp_f32_e32 v157, v157
	v_exp_f32_e32 v158, v158
	v_exp_f32_e32 v159, v159
	s_waitcnt lgkmcnt(0)
	v_mfma_f32_16x16x32_bf16 v[132:135], v[40:43], v[104:107], 0
	v_mfma_f32_16x16x32_bf16 v[132:135], v[44:47], v[108:111], v[132:135]
	v_mfma_f32_16x16x32_bf16 v[132:135], v[48:51], v[112:115], v[132:135]
	v_mfma_f32_16x16x32_bf16 v[132:135], v[52:55], v[116:119], v[132:135]
	v_mul_f32_e32 v156, v128, v156
	v_mul_f32_e32 v157, v129, v157
	v_mul_f32_e32 v158, v130, v158
	v_mul_f32_e32 v159, v131, v159
	v_sub_f32_e32 v160, v144, v139
	v_sub_f32_e32 v161, v145, v139
	v_sub_f32_e32 v162, v146, v139
	v_sub_f32_e32 v163, v147, v139
	v_mul_f32_e32 v160, s34, v160
	v_mul_f32_e32 v161, s34, v161
	v_mul_f32_e32 v162, s34, v162
	v_mul_f32_e32 v163, s34, v163
	v_exp_f32_e32 v160, v160
	v_exp_f32_e32 v161, v161
	v_exp_f32_e32 v162, v162
	v_exp_f32_e32 v163, v163
	v_mul_f32_e32 v160, v132, v160
	v_mul_f32_e32 v161, v133, v161
	v_mul_f32_e32 v162, v134, v162
	v_mul_f32_e32 v163, v135, v163
	s_and_b64 vcc, exec, s[56:57]
	s_cbranch_vccnz .Lgc_qk
	v_cmp_lt_i32_e32 vcc, v0, v12
	v_cmp_lt_i32_e64 s[0:1], v0, v13
	v_cmp_lt_i32_e64 s[20:21], v0, v14
	v_cndmask_b32_e32 v148, 0, v148, vcc
	v_cmp_lt_i32_e32 vcc, v0, v15
	v_cndmask_b32_e64 v149, 0, v149, s[0:1]
	v_cndmask_b32_e64 v150, 0, v150, s[20:21]
	s_nop 0
	v_cndmask_b32_e32 v151, 0, v151, vcc
	v_cmp_lt_i32_e32 vcc, v9, v12
	v_cmp_lt_i32_e64 s[0:1], v9, v13
	v_cmp_lt_i32_e64 s[20:21], v9, v14
	v_cndmask_b32_e32 v152, 0, v152, vcc
	v_cmp_lt_i32_e32 vcc, v9, v15
	v_cndmask_b32_e64 v153, 0, v153, s[0:1]
	v_cndmask_b32_e64 v154, 0, v154, s[20:21]
	s_nop 0
	v_cndmask_b32_e32 v155, 0, v155, vcc
	v_cmp_lt_i32_e32 vcc, v10, v12
	v_cmp_lt_i32_e64 s[0:1], v10, v13
	v_cmp_lt_i32_e64 s[20:21], v10, v14
	v_cndmask_b32_e32 v156, 0, v156, vcc
	v_cmp_lt_i32_e32 vcc, v10, v15
	v_cndmask_b32_e64 v157, 0, v157, s[0:1]
	v_cndmask_b32_e64 v158, 0, v158, s[20:21]
	s_nop 0
	v_cndmask_b32_e32 v159, 0, v159, vcc
	v_cmp_lt_i32_e32 vcc, v11, v12
	v_cmp_lt_i32_e64 s[0:1], v11, v13
	v_cmp_lt_i32_e64 s[20:21], v11, v14
	v_cndmask_b32_e32 v160, 0, v160, vcc
	v_cmp_lt_i32_e32 vcc, v11, v15
	v_cndmask_b32_e64 v161, 0, v161, s[0:1]
	v_cndmask_b32_e64 v162, 0, v162, s[20:21]
	s_nop 0
	v_cndmask_b32_e32 v163, 0, v163, vcc
	v_mul_u32_u24_e32 v16, 0x110, v0
	s_lshl_b32 s34, s9, 2
	s_add_i32 s34, s34, 0x15c00
	v_lshl_add_u32 v16, v1, 4, v16
	v_add_u32_e32 v16, s34, v16
	ds_write_b128 v16, v[148:151]
	ds_write_b128 v16, v[152:155] offset:4352
	ds_write_b128 v16, v[156:159] offset:8704
	ds_write_b128 v16, v[160:163] offset:13056
	s_cmp_lt_u32 s9, 32
	s_cbranch_scc1 .Lgc_join
	s_mul_i32 s34, s9, 0x50
	s_add_i32 s34, s34, 0x1be00
	v_mul_u32_u24_e32 v17, 0x140, v1
	v_lshl_add_u32 v17, v0, 1, v17
	v_add_u32_e32 v17, s34, v17
	v_cvt_pk_bf16_f32 v164, v148, v148
	v_cvt_pk_bf16_f32 v165, v149, v149
	v_cvt_pk_bf16_f32 v166, v150, v150
	v_cvt_pk_bf16_f32 v167, v151, v151
	v_cvt_pk_bf16_f32 v168, v152, v152
	v_cvt_pk_bf16_f32 v169, v153, v153
	v_cvt_pk_bf16_f32 v170, v154, v154
	v_cvt_pk_bf16_f32 v171, v155, v155
	ds_write_b16 v17, v164
	ds_write_b16 v17, v165 offset:80
	ds_write_b16 v17, v166 offset:160
	ds_write_b16 v17, v167 offset:240
	ds_write_b16 v17, v168 offset:32
	ds_write_b16 v17, v169 offset:112
	ds_write_b16 v17, v170 offset:192
	ds_write_b16 v17, v171 offset:272
	s_branch .Lgc_join
.Lgc_qk:
	v_cmp_le_i32_e32 vcc, v12, v0
	v_cmp_le_i32_e64 s[0:1], v13, v0
	v_cmp_le_i32_e64 s[20:21], v14, v0
	v_cndmask_b32_e32 v148, 0, v148, vcc
	v_cmp_le_i32_e32 vcc, v15, v0
	v_cndmask_b32_e64 v149, 0, v149, s[0:1]
	v_cndmask_b32_e64 v150, 0, v150, s[20:21]
	s_nop 0
	v_cndmask_b32_e32 v151, 0, v151, vcc
	v_cmp_le_i32_e32 vcc, v12, v9
	v_cmp_le_i32_e64 s[0:1], v13, v9
	v_cmp_le_i32_e64 s[20:21], v14, v9
	v_cndmask_b32_e32 v152, 0, v152, vcc
	v_cmp_le_i32_e32 vcc, v15, v9
	v_cndmask_b32_e64 v153, 0, v153, s[0:1]
	v_cndmask_b32_e64 v154, 0, v154, s[20:21]
	s_nop 0
	v_cndmask_b32_e32 v155, 0, v155, vcc
	v_cmp_le_i32_e32 vcc, v12, v10
	v_cmp_le_i32_e64 s[0:1], v13, v10
	v_cmp_le_i32_e64 s[20:21], v14, v10
	v_cndmask_b32_e32 v156, 0, v156, vcc
	v_cmp_le_i32_e32 vcc, v15, v10
	v_cndmask_b32_e64 v157, 0, v157, s[0:1]
	v_cndmask_b32_e64 v158, 0, v158, s[20:21]
	s_nop 0
	v_cndmask_b32_e32 v159, 0, v159, vcc
	v_cmp_le_i32_e32 vcc, v12, v11
	v_cmp_le_i32_e64 s[0:1], v13, v11
	v_cmp_le_i32_e64 s[20:21], v14, v11
	v_cndmask_b32_e32 v160, 0, v160, vcc
	v_cmp_le_i32_e32 vcc, v15, v11
	v_cndmask_b32_e64 v161, 0, v161, s[0:1]
	v_cndmask_b32_e64 v162, 0, v162, s[20:21]
	s_nop 0
	v_cndmask_b32_e32 v163, 0, v163, vcc
	s_add_u32 s2, s78, 0xc000
	s_addc_u32 s3, s79, 0
	s_lshl_b32 s34, s9, 6
	v_lshlrev_b32_e32 v16, 4, v0
	v_and_b32_e32 v17, 1, v1
	v_lshl_add_u32 v16, v17, 9, v16
	v_lshrrev_b32_e32 v17, 1, v1
	v_lshl_add_u32 v16, v17, 3, v16
	v_add_u32_e32 v16, s34, v16
	v_add_u32_e32 v17, 0x1000, v16
	v_cvt_pk_bf16_f32 v164, v148, v149
	v_cvt_pk_bf16_f32 v165, v150, v151
	v_cvt_pk_bf16_f32 v166, v152, v153
	v_cvt_pk_bf16_f32 v167, v154, v155
	v_cvt_pk_bf16_f32 v168, v156, v157
	v_cvt_pk_bf16_f32 v169, v158, v159
	v_cvt_pk_bf16_f32 v170, v160, v161
	v_cvt_pk_bf16_f32 v171, v162, v163
	global_store_dwordx2 v16, v[164:165], s[2:3]
	global_store_dwordx2 v16, v[166:167], s[2:3] offset:256
	global_store_dwordx2 v17, v[168:169], s[2:3]
	global_store_dwordx2 v17, v[170:171], s[2:3] offset:256
.Lgc_join:
	v_readlane_b32 s82, v253, 17
	v_readlane_b32 s83, v253, 18
	s_not_b64 s[2:3], s[56:57]
